# v38
# speedup vs baseline: 1.0101x; 1.0101x over previous
.LBB1_28:
	s_or_b64 exec, exec, s[6:7]
	s_mov_b64 s[52:53], vcc
	s_mov_b32 s41, 0x186a00
	v_cmp_gt_u32_e32 vcc, s41, v60
	s_and_saveexec_b64 s[42:43], vcc
	s_cbranch_execz .Lkb_cvv0
	v_max3_f32 v44, |v28|, 0, |v29|
	v_max3_f32 v44, v44, |v30|, |v31|
	v_max3_f32 v44, v44, |v32|, |v33|
	v_max3_f32 v44, v44, |v34|, |v35|
	s_nop 1
	v_max_f32_dpp v44, v44, v44 quad_perm:[1,0,3,2] row_mask:0xf bank_mask:0xf bound_ctrl:1
	s_nop 1
	v_max_f32_dpp v44, v44, v44 quad_perm:[2,3,0,1] row_mask:0xf bank_mask:0xf bound_ctrl:1
	s_nop 1
	v_max_f32_dpp v44, v44, v44 row_half_mirror row_mask:0xf bank_mask:0xf bound_ctrl:1
	s_nop 1
	v_max_f32_dpp v44, v44, v44 row_mirror row_mask:0xf bank_mask:0xf bound_ctrl:1
	s_mov_b32 s44, 0x42fe0000
	v_div_scale_f32 v52, s[46:47], v44, v44, s44
	v_rcp_f32_e32 v53, v52
	v_div_scale_f32 v54, vcc, s44, v44, s44
	v_fma_f32 v55, -v52, v53, 1.0
	v_fmac_f32_e32 v53, v55, v53
	v_mul_f32_e32 v55, v54, v53
	v_fma_f32 v56, -v52, v55, v54
	v_fmac_f32_e32 v55, v56, v53
	v_fma_f32 v52, -v52, v55, v54
	v_div_fmas_f32 v52, v52, v53, v55
	v_div_fixup_f32 v52, v52, v44, s44
	v_cmp_lt_f32_e32 vcc, 0, v44
	s_nop 1
	v_cndmask_b32_e32 v52, 0, v52, vcc
	v_mul_f32_e32 v28, v28, v52
	v_mul_f32_e32 v29, v29, v52
	v_mul_f32_e32 v30, v30, v52
	v_mul_f32_e32 v31, v31, v52
	v_mul_f32_e32 v32, v32, v52
	v_mul_f32_e32 v33, v33, v52
	v_mul_f32_e32 v34, v34, v52
	v_mul_f32_e32 v35, v35, v52
	v_rndne_f32_e32 v28, v28
	v_rndne_f32_e32 v29, v29
	v_rndne_f32_e32 v30, v30
	v_rndne_f32_e32 v31, v31
	v_rndne_f32_e32 v32, v32
	v_rndne_f32_e32 v33, v33
	v_rndne_f32_e32 v34, v34
	v_rndne_f32_e32 v35, v35
	v_add_f32_e32 v28, 0x43000000, v28
	v_add_f32_e32 v29, 0x43000000, v29
	v_add_f32_e32 v30, 0x43000000, v30
	v_add_f32_e32 v31, 0x43000000, v31
	v_add_f32_e32 v32, 0x43000000, v32
	v_add_f32_e32 v33, 0x43000000, v33
	v_add_f32_e32 v34, 0x43000000, v34
	v_add_f32_e32 v35, 0x43000000, v35
	v_cvt_pk_u8_f32 v46, v28, 0, 0
	v_cvt_pk_u8_f32 v47, v32, 0, 0
	v_cvt_pk_u8_f32 v46, v29, 1, v46
	v_cvt_pk_u8_f32 v47, v33, 1, v47
	v_cvt_pk_u8_f32 v46, v30, 2, v46
	v_cvt_pk_u8_f32 v47, v34, 2, v47
	v_cvt_pk_u8_f32 v46, v31, 3, v46
	v_cvt_pk_u8_f32 v47, v35, 3, v47
.Lkb_cvv0:
	s_mov_b64 exec, s[42:43]
	s_mov_b64 vcc, s[52:53]
	s_waitcnt vmcnt(0)
	v_cmp_lt_i32_e64 s[14:15], -1, v15
	s_and_saveexec_b64 s[4:5], s[14:15]
	v_lshrrev_b32_e32 v2, 15, v15
	v_and_b32_e32 v2, 0x1fffc, v2
	v_mov_b32_e32 v3, 1
	ds_add_u32 v2, v3 offset:26624
	s_or_b64 exec, exec, s[4:5]
	s_load_dwordx4 s[20:23], s[0:1], 0x10
	v_or_b32_e32 v6, 32, v1
	v_cmp_lt_i32_e64 s[0:1], v6, v24
	s_and_saveexec_b64 s[4:5], s[0:1]
	s_cbranch_execz .LBB1_33
	ds_read_b32 v2, v4 offset:25600
	s_mov_b64 s[6:7], 0
	v_mov_b32_e32 v25, 1
	s_mov_b64 s[8:9], 0x80
	v_mov_b32_e32 v26, v6
	s_waitcnt lgkmcnt(0)
	v_add3_u32 v2, v2, v1, 32
	v_ashrrev_i32_e32 v3, 31, v2
	v_lshl_add_u64 v[2:3], v[2:3], 2, s[24:25]

.LBB1_90:
	s_or_b64 exec, exec, s[2:3]
	v_mov_b32_e32 v2, 0
	s_waitcnt lgkmcnt(0)
	s_barrier
	s_add_u32 s48, s38, 0x30f4200
	s_addc_u32 s49, s39, 0
	s_add_u32 s50, s38, 0x495e400
	s_addc_u32 s51, s39, 0
	s_mov_b32 s41, 0x186a00
	v_cmp_gt_u32_e32 vcc, s41, v60
	s_and_saveexec_b64 s[42:43], vcc
	s_cbranch_execz .Lkb_cvs0
	v_lshlrev_b32_e32 v52, 3, v60
	global_store_dwordx2 v52, v[46:47], s[48:49]
	v_and_b32_e32 v53, 15, v60
	v_cmp_eq_u32_e32 vcc, 0, v53
	s_and_b64 exec, exec, vcc
	s_cbranch_execz .Lkb_cvs0
	v_mul_f32_e32 v54, 0x41010204, v44
	v_lshrrev_b32_e32 v55, 4, v60
	v_lshlrev_b32_e32 v55, 2, v55
	global_store_dword v55, v54, s[50:51]
.Lkb_cvs0:
	s_mov_b64 exec, s[42:43]
	ds_read_b32 v14, v2 offset:27716
	s_movk_i32 s2, 0x1801
	s_waitcnt lgkmcnt(0)
	v_cmp_gt_i32_e32 vcc, s2, v14
	s_mov_b64 s[2:3], -1
	s_cbranch_vccnz .LBB1_132
	s_and_saveexec_b64 s[2:3], s[14:15]
	s_cbranch_execz .LBB1_93
	v_lshrrev_b32_e32 v2, 15, v15
	v_and_b32_e32 v2, 0x1fffc, v2
	v_mov_b32_e32 v3, 1
	ds_add_rtn_u32 v2, v2, v3 offset:26624
	v_and_b32_e32 v16, 0x1ffff, v15
	s_waitcnt lgkmcnt(0)
	v_ashrrev_i32_e32 v3, 31, v2
	v_lshl_add_u64 v[2:3], v[2:3], 2, s[22:23]
	global_store_dword v[2:3], v16, off
